# nonop
# baseline (speedup 1.0000x reference)
.LBB1_12:
	s_and_b32 s12, s19, 1
	s_lshr_b32 s13, s19, 1
	s_add_i32 s16, s19, 1
	v_lshl_add_u32 v231, s13, 3, v221
	s_cmp_lg_u32 s19, 3
	s_cselect_b32 s17, s16, 3
	s_waitcnt lgkmcnt(2)
	v_lshlrev_b32_e32 v2, 7, v231
	s_lshl_b32 s14, s12, 6
	v_or3_b32 v160, v2, s14, v220
	s_waitcnt lgkmcnt(0)
	v_mov_b32_e32 v1, v220
	v_lshl_add_u64 v[2:3], v[160:161], 2, s[6:7]
	global_load_dword v232, v[2:3], off
	s_lshl_b32 s14, s17, 2
	s_and_b32 s14, s14, 24
	s_lshl_b32 s13, s13, 9
	v_lshrrev_b32_e32 v3, 5, v1
	s_cmp_eq_u32 s12, 0
	v_add_u32_e32 v2, s14, v221
	v_lshlrev_b32_e32 v206, 4, v3
	s_cselect_b64 s[14:15], -1, 0
	s_cmp_eq_u32 s12, 1
	v_add3_u32 v149, v228, s13, v206
	s_cselect_b64 s[12:13], -1, 0
	s_lshl_b32 s17, s17, 6
	s_and_b32 s17, s17, 64
	v_lshl_or_b32 v2, v2, 7, s17
	v_lshl_add_u32 v234, v1, 4, 0
	v_and_or_b32 v1, v1, 31, v2
	v_mul_lo_u32 v2, v1, 27
	v_add_u32_e32 v233, 0xc000, v234
	v_mad_u64_u32 v[204:205], s[20:21], v3, 14, v[2:3]
	v_add_u32_e32 v202, 13, v2
	s_waitcnt vmcnt(3)
	v_mul_f32_e32 v1, 0.15915494, v222
	v_cos_f32_e32 v2, v1
	v_sin_f32_e32 v1, v1
	v_add_f32_e32 v2, v2, v2
	v_cndmask_b32_e64 v3, v2, v1, s[0:1]
	v_mul_f32_e32 v1, v1, v2
	v_fma_f32 v2, v2, v2, -2.0
	v_cndmask_b32_e64 v4, v2, v1, s[0:1]
	v_mul_f32_e32 v207, v1, v2
	v_fma_f32 v208, v2, v2, -2.0
	v_mul_f32_e32 v2, 0.15915494, v182
	v_cvt_pk_fp8_f32 v131, v225, v3
	v_cos_f32_e32 v3, v2
	v_sin_f32_e32 v2, v2
	v_cndmask_b32_e64 v1, v208, v207, s[0:1]
	v_cvt_pk_fp8_f32 v131, v4, v1 op_sel:[0,0,1]
	v_add_f32_e32 v1, v3, v3
	v_cvt_pk_f16_f32 v1, v2, v1
	v_cvt_pk_fp8_f32 v128, v182, v0
	v_cvt_scalef32_pk_fp8_f16 v132, v1, 1.0
	v_pk_fma_f16 v1, v1, v1, -2.0 op_sel:[1,0,1] op_sel_hi:[1,1,0]
	v_mul_f32_e32 v0, 0.15915494, v0
	v_cvt_scalef32_pk_fp8_f16 v132, v1, 1.0 op_sel:[0,0,1]
	v_pk_fma_f16 v1, v1, v1, -2.0 op_sel:[0,1,1] op_sel_hi:[1,1,0]
	v_cos_f32_e32 v2, v0
	v_cvt_scalef32_pk_fp8_f16 v133, v1, 1.0
	v_pk_fma_f16 v1, v1, v1, -2.0 op_sel:[0,1,1] op_sel_hi:[1,1,0]
	v_sin_f32_e32 v0, v0
	v_cvt_scalef32_pk_fp8_f16 v133, v1, 1.0 op_sel:[0,0,1]
	v_pk_fma_f16 v1, v1, v1, -2.0 op_sel:[0,1,1] op_sel_hi:[1,1,0]
	v_cvt_scalef32_pk_fp8_f16 v134, v1, 1.0
	v_pk_fma_f16 v1, v1, v1, -2.0 op_sel:[0,1,1] op_sel_hi:[1,1,0]
	v_cvt_scalef32_pk_fp8_f16 v134, v1, 1.0 op_sel:[0,0,1]
	v_add_f32_e32 v1, v2, v2
	v_cvt_pk_f16_f32 v0, v0, v1
	v_cvt_scalef32_pk_fp8_f16 v135, v0, 1.0
	v_pk_fma_f16 v24, v0, v0, -2.0 op_sel:[1,0,1] op_sel_hi:[1,1,0]
	s_waitcnt vmcnt(2)
	v_mul_f32_e32 v0, 0.15915494, v224
	v_cos_f32_e32 v1, v0
	v_sin_f32_e32 v0, v0
	v_add_f32_e32 v1, v1, v1
	v_cndmask_b32_e64 v2, v1, v0, s[0:1]
	v_mul_f32_e32 v0, v0, v1
	v_fma_f32 v1, v1, v1, -2.0
	v_cndmask_b32_e64 v3, v1, v0, s[0:1]
	v_mul_f32_e32 v209, v0, v1
	v_fma_f32 v210, v1, v1, -2.0
	v_mul_f32_e32 v1, 0.15915494, v190
	s_waitcnt vmcnt(1)
	v_cvt_pk_fp8_f32 v19, v223, v2
	v_cos_f32_e32 v2, v1
	v_sin_f32_e32 v1, v1
	v_cndmask_b32_e64 v0, v210, v209, s[0:1]
	v_cvt_pk_fp8_f32 v19, v3, v0 op_sel:[0,0,1]
	v_add_f32_e32 v0, v2, v2
	v_cvt_pk_f16_f32 v0, v1, v0
	v_cvt_scalef32_pk_fp8_f16 v20, v0, 1.0
	v_pk_fma_f16 v0, v0, v0, -2.0 op_sel:[1,0,1] op_sel_hi:[1,1,0]
	v_mul_f32_e32 v1, 0.15915494, v191
	v_cvt_scalef32_pk_fp8_f16 v135, v24, 1.0 op_sel:[0,0,1]
	v_cvt_scalef32_pk_fp8_f16 v20, v0, 1.0 op_sel:[0,0,1]
	v_pk_fma_f16 v0, v0, v0, -2.0 op_sel:[0,1,1] op_sel_hi:[1,1,0]
	v_cos_f32_e32 v2, v1
	v_pk_fma_f16 v24, v24, v24, -2.0 op_sel:[0,1,1] op_sel_hi:[1,1,0]
	v_cvt_scalef32_pk_fp8_f16 v21, v0, 1.0
	v_pk_fma_f16 v0, v0, v0, -2.0 op_sel:[0,1,1] op_sel_hi:[1,1,0]
	v_sin_f32_e32 v1, v1
	v_pk_fma_f16 v35, v24, v24, -2.0 op_sel:[0,1,1] op_sel_hi:[1,1,0]
	v_cvt_pk_fp8_f32 v128, v25, v185 op_sel:[0,0,1]
	v_cvt_scalef32_pk_fp8_f16 v21, v0, 1.0 op_sel:[0,0,1]
	v_pk_fma_f16 v0, v0, v0, -2.0 op_sel:[0,1,1] op_sel_hi:[1,1,0]
	v_pk_fma_f16 v36, v35, v35, -2.0 op_sel:[0,1,1] op_sel_hi:[1,1,0]
	v_mul_f32_e32 v25, 0.15915494, v25
	v_cvt_pk_fp8_f32 v129, v198, v162
	v_cvt_pk_fp8_f32 v130, v178, v200
	v_cvt_pk_fp8_f32 v16, v190, v191
	v_cvt_pk_fp8_f32 v17, v194, v195
	v_cvt_pk_fp8_f32 v18, v186, v187
	v_cvt_scalef32_pk_fp8_f16 v22, v0, 1.0
	v_pk_fma_f16 v0, v0, v0, -2.0 op_sel:[0,1,1] op_sel_hi:[1,1,0]
	v_pk_fma_f16 v37, v36, v36, -2.0 op_sel:[0,1,1] op_sel_hi:[1,1,0]
	v_cvt_scalef32_pk_fp8_f16 v137, v36, 1.0
	v_cos_f32_e32 v36, v25
	v_cvt_scalef32_pk_fp8_f16 v22, v0, 1.0 op_sel:[0,0,1]
	v_add_f32_e32 v0, v2, v2
	v_sin_f32_e32 v25, v25
	v_cvt_pk_f16_f32 v0, v1, v0
	v_mov_b32_e32 v160, v204
	v_cvt_scalef32_pk_fp8_f16 v23, v0, 1.0
	v_pk_fma_f16 v34, v0, v0, -2.0 op_sel:[1,0,1] op_sel_hi:[1,1,0]
	ds_read_b128 v[26:29], v234
	ds_read_b128 v[30:33], v234 offset:1024
	ds_read_b128 v[8:11], v234 offset:2048
	ds_read_b128 v[12:15], v234 offset:3072
	ds_read_b128 v[0:3], v234 offset:4096
	ds_read_b128 v[4:7], v234 offset:5120
	ds_read_b128 v[152:155], v234 offset:6144
	ds_read_b128 v[156:159], v234 offset:7168
	ds_read_b128 v[96:99], v149
	ds_read_b128 v[100:103], v149 offset:32
	ds_read_b128 v[104:107], v149 offset:64
	ds_read_b128 v[108:111], v149 offset:96
	v_cvt_pk_fp8_f32 v129, v163, v201 op_sel:[0,0,1]
	v_cvt_pk_fp8_f32 v130, v179, v181 op_sel:[0,0,1]
	v_cvt_pk_fp8_f32 v16, v192, v193 op_sel:[0,0,1]
	v_cvt_pk_fp8_f32 v17, v196, v197 op_sel:[0,0,1]
	v_cvt_pk_fp8_f32 v18, v188, v189 op_sel:[0,0,1]
	v_cvt_scalef32_pk_fp8_f16 v136, v24, 1.0
	v_add_f32_e32 v24, v36, v36
	v_cvt_pk_f16_f32 v24, v25, v24
	v_pk_fma_f16 v25, v24, v24, -2.0 op_sel:[1,0,1] op_sel_hi:[1,1,0]
	v_cvt_scalef32_pk_fp8_f16 v138, v24, 1.0
	v_cvt_scalef32_pk_fp8_f16 v23, v34, 1.0 op_sel:[0,0,1]
	v_cvt_scalef32_pk_fp8_f16 v136, v35, 1.0 op_sel:[0,0,1]
	v_pk_fma_f16 v35, v25, v25, -2.0 op_sel:[0,1,1] op_sel_hi:[1,1,0]
	v_cvt_scalef32_pk_fp8_f16 v138, v25, 1.0 op_sel:[0,0,1]
	v_mul_f32_e32 v25, 0.15915494, v185
	s_waitcnt lgkmcnt(0)
	v_mfma_scale_f32_32x32x64_f8f6f4 v[112:127], v[26:33], v[16:23], v[96:111], v227, v226 op_sel_hi:[0,0,0]
	v_cvt_scalef32_pk_fp8_f16 v139, v35, 1.0
	v_pk_fma_f16 v35, v35, v35, -2.0 op_sel:[0,1,1] op_sel_hi:[1,1,0]
	v_pk_fma_f16 v24, v35, v35, -2.0 op_sel:[0,1,1] op_sel_hi:[1,1,0]
	ds_read_b128 v[64:67], v149 offset:128
	ds_read_b128 v[68:71], v149 offset:160
	ds_read_b128 v[72:75], v149 offset:192
	ds_read_b128 v[76:79], v149 offset:224
	v_cvt_scalef32_pk_fp8_f16 v140, v24, 1.0
	v_pk_fma_f16 v24, v24, v24, -2.0 op_sel:[0,1,1] op_sel_hi:[1,1,0]
	v_cvt_scalef32_pk_fp8_f16 v137, v37, 1.0 op_sel:[0,0,1]
	v_cvt_scalef32_pk_fp8_f16 v140, v24, 1.0 op_sel:[0,0,1]
	v_cvt_scalef32_pk_fp8_f16 v139, v35, 1.0 op_sel:[0,0,1]
	v_mfma_scale_f32_32x32x64_f8f6f4 v[96:111], v[26:33], v[128:135], v[96:111], v227, v226 op_sel_hi:[0,0,0]
	v_cos_f32_e32 v26, v25
	v_sin_f32_e32 v25, v25
	v_mul_f32_e32 v30, 0.15915494, v192
	v_mul_f32_e32 v31, 0.15915494, v193
	v_add_f32_e32 v24, v26, v26
	v_cvt_pk_f16_f32 v24, v25, v24
	v_cvt_scalef32_pk_fp8_f16 v141, v24, 1.0
	v_pk_fma_f16 v24, v24, v24, -2.0 op_sel:[1,0,1] op_sel_hi:[1,1,0]
	v_cvt_scalef32_pk_fp8_f16 v141, v24, 1.0 op_sel:[0,0,1]
	v_pk_fma_f16 v26, v24, v24, -2.0 op_sel:[0,1,1] op_sel_hi:[1,1,0]
	v_lshl_add_u64 v[24:25], v[160:161], 2, s[4:5]
	v_pk_fma_f16 v27, v26, v26, -2.0 op_sel:[0,1,1] op_sel_hi:[1,1,0]
	v_pk_fma_f16 v28, v27, v27, -2.0 op_sel:[0,1,1] op_sel_hi:[1,1,0]
	s_waitcnt lgkmcnt(0)
	v_mfma_scale_f32_32x32x64_f8f6f4 v[80:95], v[8:15], v[16:23], v[64:79], v227, v226 op_sel_hi:[0,0,0]
	global_load_dwordx4 v[182:185], v[24:25], off
	global_load_dwordx4 v[190:193], v[24:25], off offset:3456
	v_cos_f32_e32 v25, v31
	v_pk_fma_f16 v29, v28, v28, -2.0 op_sel:[0,1,1] op_sel_hi:[1,1,0]
	v_cvt_scalef32_pk_fp8_f16 v143, v28, 1.0
	v_cvt_scalef32_pk_fp8_f16 v142, v26, 1.0
	v_cvt_scalef32_pk_fp8_f16 v143, v29, 1.0 op_sel:[0,0,1]
	v_cvt_scalef32_pk_fp8_f16 v142, v27, 1.0 op_sel:[0,0,1]
	v_add_f32_e32 v150, v25, v25
	v_mfma_scale_f32_32x32x64_f8f6f4 v[64:79], v[8:15], v[128:135], v[64:79], v227, v226 op_sel_hi:[0,0,0]
	v_pk_fma_f16 v8, v34, v34, -2.0 op_sel:[0,1,1] op_sel_hi:[1,1,0]
	ds_read_b128 v[32:35], v149 offset:256
	ds_read_b128 v[36:39], v149 offset:288
	ds_read_b128 v[40:43], v149 offset:320
	ds_read_b128 v[44:47], v149 offset:352
	v_pk_fma_f16 v9, v8, v8, -2.0 op_sel:[0,1,1] op_sel_hi:[1,1,0]
	v_cvt_scalef32_pk_fp8_f16 v144, v8, 1.0
	v_pk_fma_f16 v10, v9, v9, -2.0 op_sel:[0,1,1] op_sel_hi:[1,1,0]
	v_cvt_scalef32_pk_fp8_f16 v144, v9, 1.0 op_sel:[0,0,1]
	v_pk_fma_f16 v11, v10, v10, -2.0 op_sel:[0,1,1] op_sel_hi:[1,1,0]
	v_cvt_scalef32_pk_fp8_f16 v145, v10, 1.0
	v_cos_f32_e32 v10, v30
	v_cvt_scalef32_pk_fp8_f16 v145, v11, 1.0 op_sel:[0,0,1]
	v_sin_f32_e32 v11, v30
	v_add_f32_e32 v8, v10, v10
	v_cvt_pk_f16_f32 v8, v11, v8
	v_pk_fma_f16 v9, v8, v8, -2.0 op_sel:[1,0,1] op_sel_hi:[1,1,0]
	v_cvt_scalef32_pk_fp8_f16 v146, v8, 1.0
	v_pk_fma_f16 v10, v9, v9, -2.0 op_sel:[0,1,1] op_sel_hi:[1,1,0]
	s_waitcnt lgkmcnt(0)
	v_mfma_scale_f32_32x32x64_f8f6f4 v[48:63], v[0:7], v[16:23], v[32:47], v227, v226 op_sel_hi:[0,0,0]
	v_cvt_scalef32_pk_fp8_f16 v147, v10, 1.0
	v_pk_fma_f16 v10, v10, v10, -2.0 op_sel:[0,1,1] op_sel_hi:[1,1,0]
	v_cvt_scalef32_pk_fp8_f16 v146, v9, 1.0 op_sel:[0,0,1]
	v_cvt_scalef32_pk_fp8_f16 v147, v10, 1.0 op_sel:[0,0,1]
	v_pk_fma_f16 v24, v10, v10, -2.0 op_sel:[0,1,1] op_sel_hi:[1,1,0]
	v_cvt_scalef32_pk_fp8_f16 v148, v24, 1.0
	v_pk_fma_f16 v24, v24, v24, -2.0 op_sel:[0,1,1] op_sel_hi:[1,1,0]
	v_cvt_scalef32_pk_fp8_f16 v148, v24, 1.0 op_sel:[0,0,1]
	v_mfma_scale_f32_32x32x64_f8f6f4 v[32:47], v[0:7], v[128:135], v[32:47], v227, v226 op_sel_hi:[0,0,0]
	ds_read_b128 v[0:3], v149 offset:384
	ds_read_b128 v[4:7], v149 offset:416
	ds_read_b128 v[8:11], v149 offset:448
	ds_read_b128 v[12:15], v149 offset:480
	v_sin_f32_e32 v149, v31
	s_nop 0
	v_cvt_pk_f16_f32 v150, v149, v150
	v_cvt_scalef32_pk_fp8_f16 v149, v150, 1.0
	v_pk_fma_f16 v150, v150, v150, -2.0 op_sel:[1,0,1] op_sel_hi:[1,1,0]
	v_pk_fma_f16 v160, v150, v150, -2.0 op_sel:[0,1,1] op_sel_hi:[1,1,0]
	v_cvt_scalef32_pk_fp8_f16 v149, v150, 1.0 op_sel:[0,0,1]
	v_pk_fma_f16 v164, v160, v160, -2.0 op_sel:[0,1,1] op_sel_hi:[1,1,0]
	v_pk_fma_f16 v150, v164, v164, -2.0 op_sel:[0,1,1] op_sel_hi:[1,1,0]
	s_waitcnt lgkmcnt(0)
	v_mfma_scale_f32_32x32x64_f8f6f4 v[16:31], v[152:159], v[16:23], v[0:15], v227, v226 op_sel_hi:[0,0,0]
	v_pk_fma_f16 v165, v150, v150, -2.0 op_sel:[0,1,1] op_sel_hi:[1,1,0]
	v_cvt_scalef32_pk_fp8_f16 v151, v150, 1.0
	v_cvt_scalef32_pk_fp8_f16 v150, v160, 1.0
	v_cvt_scalef32_pk_fp8_f16 v151, v165, 1.0 op_sel:[0,0,1]
	v_cvt_scalef32_pk_fp8_f16 v150, v164, 1.0 op_sel:[0,0,1]
	v_mfma_scale_f32_32x32x64_f8f6f4 v[0:15], v[152:159], v[128:135], v[0:15], v227, v226 op_sel_hi:[0,0,0]
	v_mul_f32_e32 v128, 0.15915494, v198
	v_cos_f32_e32 v129, v128
	v_sin_f32_e32 v128, v128
	v_mul_f32_e32 v133, 0.15915494, v162
	v_cos_f32_e32 v134, v133
	v_add_f32_e32 v129, v129, v129
	v_cvt_pk_f16_f32 v130, v128, v129
	v_pk_fma_f16 v131, v130, v130, -2.0 op_sel:[1,0,1] op_sel_hi:[1,1,0]
	v_sin_f32_e32 v133, v133
	v_pk_fma_f16 v128, v131, v131, -2.0 op_sel:[0,1,1] op_sel_hi:[1,1,0]
	v_pk_fma_f16 v132, v128, v128, -2.0 op_sel:[0,1,1] op_sel_hi:[1,1,0]
	v_cvt_scalef32_pk_fp8_f16 v129, v128, 1.0
	v_cvt_scalef32_pk_fp8_f16 v128, v130, 1.0
	v_add_f32_e32 v130, v134, v134
	v_cvt_scalef32_pk_fp8_f16 v128, v131, 1.0 op_sel:[0,0,1]
	v_cvt_pk_f16_f32 v130, v133, v130
	v_cvt_scalef32_pk_fp8_f16 v129, v132, 1.0 op_sel:[0,0,1]
	v_cvt_scalef32_pk_fp8_f16 v131, v130, 1.0
	v_pk_fma_f16 v133, v130, v130, -2.0 op_sel:[1,0,1] op_sel_hi:[1,1,0]
	v_pk_fma_f16 v132, v132, v132, -2.0 op_sel:[0,1,1] op_sel_hi:[1,1,0]
	ds_read_b128 v[152:155], v234 offset:8192
	ds_read_b128 v[156:159], v234 offset:9216
	ds_read_b128 v[164:167], v234 offset:10240
	ds_read_b128 v[168:171], v234 offset:11264
	ds_read_b128 v[236:239], v234 offset:12288
	ds_read_b128 v[240:243], v234 offset:13312
	v_cvt_scalef32_pk_fp8_f16 v130, v132, 1.0
	v_pk_fma_f16 v132, v132, v132, -2.0 op_sel:[0,1,1] op_sel_hi:[1,1,0]
	v_mul_f32_e32 v135, 0.15915494, v163
	s_waitcnt lgkmcnt(4)
	v_mfma_scale_f32_32x32x64_f8f6f4 v[96:111], v[152:159], v[136:143], v[96:111], v227, v226 op_sel_hi:[0,0,0]
	v_cvt_scalef32_pk_fp8_f16 v131, v133, 1.0 op_sel:[0,0,1]
	v_pk_fma_f16 v133, v133, v133, -2.0 op_sel:[0,1,1] op_sel_hi:[1,1,0]
	v_cvt_scalef32_pk_fp8_f16 v130, v132, 1.0 op_sel:[0,0,1]
	v_cvt_scalef32_pk_fp8_f16 v132, v133, 1.0
	v_pk_fma_f16 v133, v133, v133, -2.0 op_sel:[0,1,1] op_sel_hi:[1,1,0]
	ds_read_b128 v[244:247], v234 offset:14336
	ds_read_b128 v[248:251], v234 offset:15360
	v_pk_fma_f16 v134, v133, v133, -2.0 op_sel:[0,1,1] op_sel_hi:[1,1,0]
	v_cvt_scalef32_pk_fp8_f16 v132, v133, 1.0 op_sel:[0,0,1]
	v_cvt_scalef32_pk_fp8_f16 v133, v134, 1.0
	v_pk_fma_f16 v134, v134, v134, -2.0 op_sel:[0,1,1] op_sel_hi:[1,1,0]
	v_cvt_scalef32_pk_fp8_f16 v133, v134, 1.0 op_sel:[0,0,1]
	v_mfma_scale_f32_32x32x64_f8f6f4 v[112:127], v[152:159], v[144:151], v[112:127], v227, v226 op_sel_hi:[0,0,0]
	v_cos_f32_e32 v152, v135
	v_sin_f32_e32 v135, v135
	v_mul_f32_e32 v154, 0.15915494, v194
	v_cos_f32_e32 v155, v154
	v_add_f32_e32 v134, v152, v152
	v_cvt_pk_f16_f32 v152, v135, v134
	v_pk_fma_f16 v153, v152, v152, -2.0 op_sel:[1,0,1] op_sel_hi:[1,1,0]
	v_sin_f32_e32 v154, v154
	v_pk_fma_f16 v134, v153, v153, -2.0 op_sel:[0,1,1] op_sel_hi:[1,1,0]
	v_pk_fma_f16 v160, v134, v134, -2.0 op_sel:[0,1,1] op_sel_hi:[1,1,0]
	v_cvt_scalef32_pk_fp8_f16 v135, v134, 1.0
	v_cvt_scalef32_pk_fp8_f16 v134, v152, 1.0
	v_add_f32_e32 v152, v155, v155
	s_waitcnt lgkmcnt(4)
	v_mfma_scale_f32_32x32x64_f8f6f4 v[64:79], v[164:171], v[136:143], v[64:79], v227, v226 op_sel_hi:[0,0,0]
	v_mul_f32_e32 v157, 0.15915494, v195
	v_cvt_pk_f16_f32 v154, v154, v152
	v_cos_f32_e32 v158, v157
	v_pk_fma_f16 v155, v154, v154, -2.0 op_sel:[1,0,1] op_sel_hi:[1,1,0]
	v_sin_f32_e32 v157, v157
	v_pk_fma_f16 v152, v155, v155, -2.0 op_sel:[0,1,1] op_sel_hi:[1,1,0]
	v_cvt_scalef32_pk_fp8_f16 v134, v153, 1.0 op_sel:[0,0,1]
	v_pk_fma_f16 v156, v152, v152, -2.0 op_sel:[0,1,1] op_sel_hi:[1,1,0]
	v_cvt_scalef32_pk_fp8_f16 v153, v152, 1.0
	v_cvt_scalef32_pk_fp8_f16 v152, v154, 1.0
	v_add_f32_e32 v154, v158, v158
	v_mul_f32_e32 v159, 0.15915494, v196
	v_cvt_scalef32_pk_fp8_f16 v152, v155, 1.0 op_sel:[0,0,1]
	v_mfma_scale_f32_32x32x64_f8f6f4 v[80:95], v[164:171], v[144:151], v[80:95], v227, v226 op_sel_hi:[0,0,0]
	v_cvt_pk_f16_f32 v154, v157, v154
	v_cvt_scalef32_pk_fp8_f16 v153, v156, 1.0 op_sel:[0,0,1]
	v_cvt_scalef32_pk_fp8_f16 v155, v154, 1.0
	v_pk_fma_f16 v156, v156, v156, -2.0 op_sel:[0,1,1] op_sel_hi:[1,1,0]
	v_pk_fma_f16 v157, v154, v154, -2.0 op_sel:[1,0,1] op_sel_hi:[1,1,0]
	v_cvt_scalef32_pk_fp8_f16 v154, v156, 1.0
	v_pk_fma_f16 v156, v156, v156, -2.0 op_sel:[0,1,1] op_sel_hi:[1,1,0]
	v_cvt_scalef32_pk_fp8_f16 v155, v157, 1.0 op_sel:[0,0,1]
	v_pk_fma_f16 v157, v157, v157, -2.0 op_sel:[0,1,1] op_sel_hi:[1,1,0]
	v_cvt_scalef32_pk_fp8_f16 v154, v156, 1.0 op_sel:[0,0,1]
	v_cvt_scalef32_pk_fp8_f16 v156, v157, 1.0
	v_pk_fma_f16 v157, v157, v157, -2.0 op_sel:[0,1,1] op_sel_hi:[1,1,0]
	s_waitcnt lgkmcnt(0)
	v_mfma_scale_f32_32x32x64_f8f6f4 v[0:15], v[244:251], v[136:143], v[0:15], v227, v226 op_sel_hi:[0,0,0]
	v_cvt_scalef32_pk_fp8_f16 v156, v157, 1.0 op_sel:[0,0,1]
	v_pk_fma_f16 v158, v157, v157, -2.0 op_sel:[0,1,1] op_sel_hi:[1,1,0]
	v_cvt_scalef32_pk_fp8_f16 v135, v160, 1.0 op_sel:[0,0,1]
	v_cvt_scalef32_pk_fp8_f16 v157, v158, 1.0
	v_mfma_scale_f32_32x32x64_f8f6f4 v[32:47], v[236:243], v[136:143], v[32:47], v227, v226 op_sel_hi:[0,0,0]
	v_cos_f32_e32 v136, v159
	v_sin_f32_e32 v137, v159
	v_pk_fma_f16 v138, v158, v158, -2.0 op_sel:[0,1,1] op_sel_hi:[1,1,0]
	v_add_f32_e32 v136, v136, v136
	v_cvt_pk_f16_f32 v136, v137, v136
	v_pk_fma_f16 v137, v136, v136, -2.0 op_sel:[1,0,1] op_sel_hi:[1,1,0]
	v_cvt_scalef32_pk_fp8_f16 v157, v138, 1.0 op_sel:[0,0,1]
	v_pk_fma_f16 v138, v137, v137, -2.0 op_sel:[0,1,1] op_sel_hi:[1,1,0]
	v_pk_fma_f16 v180, v138, v138, -2.0 op_sel:[0,1,1] op_sel_hi:[1,1,0]
	v_cvt_scalef32_pk_fp8_f16 v159, v138, 1.0
	v_cvt_scalef32_pk_fp8_f16 v158, v136, 1.0
	v_cvt_scalef32_pk_fp8_f16 v159, v180, 1.0 op_sel:[0,0,1]
	v_cvt_scalef32_pk_fp8_f16 v158, v137, 1.0 op_sel:[0,0,1]
	v_mfma_scale_f32_32x32x64_f8f6f4 v[48:63], v[236:243], v[144:151], v[48:63], v227, v226 op_sel_hi:[0,0,0]
	v_mfma_scale_f32_32x32x64_f8f6f4 v[16:31], v[244:251], v[144:151], v[16:31], v227, v226 op_sel_hi:[0,0,0]
	ds_read_b128 v[140:143], v234 offset:16384
	ds_read_b128 v[144:147], v234 offset:17408
	ds_read_b128 v[236:239], v234 offset:18432
	ds_read_b128 v[240:243], v234 offset:19456
	ds_read_b128 v[170:173], v234 offset:20480
	ds_read_b128 v[174:177], v234 offset:21504
	s_waitcnt lgkmcnt(4)
	v_mfma_scale_f32_32x32x64_f8f6f4 v[96:111], v[140:147], v[128:135], v[96:111], v227, v226 op_sel_hi:[0,0,0]
	v_pk_fma_f16 v139, v160, v160, -2.0 op_sel:[0,1,1] op_sel_hi:[1,1,0]
	v_mov_b32_e32 v160, v204
	ds_read_b128 v[162:165], v234 offset:22528
	ds_read_b128 v[166:169], v234 offset:23552
	v_mul_f32_e32 v136, 0.15915494, v201
	v_cos_f32_e32 v137, v136
	v_sin_f32_e32 v136, v136
	v_mul_f32_e32 v150, 0.15915494, v186
	v_cos_f32_e32 v151, v150
	v_add_f32_e32 v137, v137, v137
	v_cvt_pk_f16_f32 v136, v136, v137
	v_pk_fma_f16 v138, v136, v136, -2.0 op_sel:[1,0,1] op_sel_hi:[1,1,0]
	v_cvt_scalef32_pk_fp8_f16 v137, v136, 1.0
	v_mfma_scale_f32_32x32x64_f8f6f4 v[112:127], v[140:147], v[152:159], v[112:127], v227, v226 op_sel_hi:[0,0,0]
	v_mul_f32_e32 v140, 0.15915494, v178
	v_cos_f32_e32 v141, v140
	v_sin_f32_e32 v140, v140
	v_mul_f32_e32 v143, 0.15915494, v200
	v_cos_f32_e32 v144, v143
	v_add_f32_e32 v141, v141, v141
	v_cvt_pk_f16_f32 v141, v140, v141
	v_sin_f32_e32 v143, v143
	v_cvt_scalef32_pk_fp8_f16 v140, v141, 1.0
	v_pk_fma_f16 v141, v141, v141, -2.0 op_sel:[1,0,1] op_sel_hi:[1,1,0]
	v_mul_f32_e32 v146, 0.15915494, v197
	v_pk_fma_f16 v142, v141, v141, -2.0 op_sel:[0,1,1] op_sel_hi:[1,1,0]
	v_cvt_scalef32_pk_fp8_f16 v140, v141, 1.0 op_sel:[0,0,1]
	v_cvt_scalef32_pk_fp8_f16 v141, v142, 1.0
	v_pk_fma_f16 v145, v142, v142, -2.0 op_sel:[0,1,1] op_sel_hi:[1,1,0]
	v_add_f32_e32 v142, v144, v144
	v_cvt_pk_f16_f32 v144, v143, v142
	v_lshl_add_u64 v[142:143], v[160:161], 2, s[4:5]
	global_load_dwordx4 v[198:201], v[142:143], off offset:16
	global_load_dwordx4 v[194:197], v[142:143], off offset:3472
	v_cvt_scalef32_pk_fp8_f16 v141, v145, 1.0 op_sel:[0,0,1]
	v_pk_fma_f16 v160, v144, v144, -2.0 op_sel:[1,0,1] op_sel_hi:[1,1,0]
	v_cvt_scalef32_pk_fp8_f16 v143, v144, 1.0
	v_pk_fma_f16 v144, v145, v145, -2.0 op_sel:[0,1,1] op_sel_hi:[1,1,0]
	v_cos_f32_e32 v145, v146
	v_sin_f32_e32 v146, v146
	v_pk_fma_f16 v148, v138, v138, -2.0 op_sel:[0,1,1] op_sel_hi:[1,1,0]
	v_cvt_scalef32_pk_fp8_f16 v136, v139, 1.0
	v_pk_fma_f16 v139, v139, v139, -2.0 op_sel:[0,1,1] op_sel_hi:[1,1,0]
	v_pk_fma_f16 v149, v148, v148, -2.0 op_sel:[0,1,1] op_sel_hi:[1,1,0]
	v_cvt_scalef32_pk_fp8_f16 v142, v144, 1.0
	v_pk_fma_f16 v144, v144, v144, -2.0 op_sel:[0,1,1] op_sel_hi:[1,1,0]
	v_cvt_scalef32_pk_fp8_f16 v137, v138, 1.0 op_sel:[0,0,1]
	v_cvt_scalef32_pk_fp8_f16 v136, v139, 1.0 op_sel:[0,0,1]
	v_pk_fma_f16 v138, v149, v149, -2.0 op_sel:[0,1,1] op_sel_hi:[1,1,0]
	v_cvt_scalef32_pk_fp8_f16 v142, v144, 1.0 op_sel:[0,0,1]
	v_add_f32_e32 v144, v145, v145
	v_cvt_scalef32_pk_fp8_f16 v139, v138, 1.0
	v_pk_fma_f16 v138, v138, v138, -2.0 op_sel:[0,1,1] op_sel_hi:[1,1,0]
	s_waitcnt lgkmcnt(4)
	v_mfma_scale_f32_32x32x64_f8f6f4 v[64:79], v[236:243], v[128:135], v[64:79], v227, v226 op_sel_hi:[0,0,0]
	v_cvt_pk_f16_f32 v144, v146, v144
	v_cvt_scalef32_pk_fp8_f16 v139, v138, 1.0 op_sel:[0,0,1]
	v_pk_fma_f16 v146, v144, v144, -2.0 op_sel:[1,0,1] op_sel_hi:[1,1,0]
	v_cvt_scalef32_pk_fp8_f16 v138, v148, 1.0
	v_cvt_scalef32_pk_fp8_f16 v145, v144, 1.0
	v_pk_fma_f16 v147, v180, v180, -2.0 op_sel:[0,1,1] op_sel_hi:[1,1,0]
	v_pk_fma_f16 v148, v146, v146, -2.0 op_sel:[0,1,1] op_sel_hi:[1,1,0]
	v_cvt_scalef32_pk_fp8_f16 v138, v149, 1.0 op_sel:[0,0,1]
	v_cvt_scalef32_pk_fp8_f16 v144, v147, 1.0
	v_pk_fma_f16 v147, v147, v147, -2.0 op_sel:[0,1,1] op_sel_hi:[1,1,0]
	v_pk_fma_f16 v149, v148, v148, -2.0 op_sel:[0,1,1] op_sel_hi:[1,1,0]
	v_cvt_scalef32_pk_fp8_f16 v145, v146, 1.0 op_sel:[0,0,1]
	v_mfma_scale_f32_32x32x64_f8f6f4 v[80:95], v[236:243], v[152:159], v[80:95], v227, v226 op_sel_hi:[0,0,0]
	v_pk_fma_f16 v146, v149, v149, -2.0 op_sel:[0,1,1] op_sel_hi:[1,1,0]
	v_cvt_scalef32_pk_fp8_f16 v144, v147, 1.0 op_sel:[0,0,1]
	v_cvt_scalef32_pk_fp8_f16 v147, v146, 1.0
	v_pk_fma_f16 v146, v146, v146, -2.0 op_sel:[0,1,1] op_sel_hi:[1,1,0]
	v_sin_f32_e32 v150, v150
	v_cvt_scalef32_pk_fp8_f16 v147, v146, 1.0 op_sel:[0,0,1]
	v_cvt_scalef32_pk_fp8_f16 v146, v148, 1.0
	v_add_f32_e32 v148, v151, v151
	v_mul_f32_e32 v151, 0.15915494, v187
	v_cvt_scalef32_pk_fp8_f16 v146, v149, 1.0 op_sel:[0,0,1]
	v_cvt_pk_f16_f32 v149, v150, v148
	v_cvt_scalef32_pk_fp8_f16 v148, v149, 1.0
	s_waitcnt lgkmcnt(0)
	v_mfma_scale_f32_32x32x64_f8f6f4 v[0:15], v[162:169], v[128:135], v[0:15], v227, v226 op_sel_hi:[0,0,0]
	v_pk_fma_f16 v149, v149, v149, -2.0 op_sel:[1,0,1] op_sel_hi:[1,1,0]
	v_cvt_scalef32_pk_fp8_f16 v143, v160, 1.0 op_sel:[0,0,1]
	v_pk_fma_f16 v150, v149, v149, -2.0 op_sel:[0,1,1] op_sel_hi:[1,1,0]
	v_cvt_scalef32_pk_fp8_f16 v148, v149, 1.0 op_sel:[0,0,1]
	v_cvt_scalef32_pk_fp8_f16 v149, v150, 1.0
	v_mfma_scale_f32_32x32x64_f8f6f4 v[32:47], v[170:177], v[128:135], v[32:47], v227, v226 op_sel_hi:[0,0,0]
	v_cos_f32_e32 v128, v151
	v_sin_f32_e32 v129, v151
	v_pk_fma_f16 v130, v150, v150, -2.0 op_sel:[0,1,1] op_sel_hi:[1,1,0]
	v_add_f32_e32 v128, v128, v128
	v_cvt_pk_f16_f32 v128, v129, v128
	v_pk_fma_f16 v203, v128, v128, -2.0 op_sel:[1,0,1] op_sel_hi:[1,1,0]
	v_cvt_scalef32_pk_fp8_f16 v151, v128, 1.0
	v_pk_fma_f16 v128, v130, v130, -2.0 op_sel:[0,1,1] op_sel_hi:[1,1,0]
	v_cvt_scalef32_pk_fp8_f16 v150, v128, 1.0
	v_pk_fma_f16 v128, v128, v128, -2.0 op_sel:[0,1,1] op_sel_hi:[1,1,0]
	v_cvt_scalef32_pk_fp8_f16 v149, v130, 1.0 op_sel:[0,0,1]
	v_cvt_scalef32_pk_fp8_f16 v151, v203, 1.0 op_sel:[0,0,1]
	v_cvt_scalef32_pk_fp8_f16 v150, v128, 1.0 op_sel:[0,0,1]
	v_mfma_scale_f32_32x32x64_f8f6f4 v[48:63], v[170:177], v[152:159], v[48:63], v227, v226 op_sel_hi:[0,0,0]
	v_mfma_scale_f32_32x32x64_f8f6f4 v[16:31], v[162:169], v[152:159], v[16:31], v227, v226 op_sel_hi:[0,0,0]
	v_pk_fma_f16 v130, v160, v160, -2.0 op_sel:[0,1,1] op_sel_hi:[1,1,0]
	v_pk_fma_f16 v131, v130, v130, -2.0 op_sel:[0,1,1] op_sel_hi:[1,1,0]
	ds_read_b128 v[152:155], v234 offset:24576
	ds_read_b128 v[156:159], v234 offset:25600
	ds_read_b128 v[162:165], v234 offset:26624
	ds_read_b128 v[166:169], v234 offset:27648
	v_pk_fma_f16 v128, v131, v131, -2.0 op_sel:[0,1,1] op_sel_hi:[1,1,0]
	v_mov_b32_e32 v160, v204
	v_pk_fma_f16 v132, v128, v128, -2.0 op_sel:[0,1,1] op_sel_hi:[1,1,0]
	v_cvt_scalef32_pk_fp8_f16 v129, v128, 1.0
	v_cvt_scalef32_pk_fp8_f16 v129, v132, 1.0 op_sel:[0,0,1]
	v_mul_f32_e32 v132, 0.15915494, v179
	v_sin_f32_e32 v133, v132
	v_cos_f32_e32 v132, v132
	v_cvt_scalef32_pk_fp8_f16 v128, v130, 1.0
	v_cvt_scalef32_pk_fp8_f16 v128, v131, 1.0 op_sel:[0,0,1]
	v_add_f32_e32 v130, v132, v132
	v_cvt_pk_f16_f32 v132, v133, v130
	v_pk_fma_f16 v133, v132, v132, -2.0 op_sel:[1,0,1] op_sel_hi:[1,1,0]
	v_pk_fma_f16 v130, v133, v133, -2.0 op_sel:[0,1,1] op_sel_hi:[1,1,0]
	s_waitcnt lgkmcnt(2)
	v_mfma_scale_f32_32x32x64_f8f6f4 v[96:111], v[152:159], v[136:143], v[96:111], v227, v226 op_sel_hi:[0,0,0]
	v_cvt_scalef32_pk_fp8_f16 v131, v130, 1.0
	v_pk_fma_f16 v134, v130, v130, -2.0 op_sel:[0,1,1] op_sel_hi:[1,1,0]
	v_cvt_scalef32_pk_fp8_f16 v130, v132, 1.0
	v_cvt_scalef32_pk_fp8_f16 v131, v134, 1.0 op_sel:[0,0,1]
	v_cvt_scalef32_pk_fp8_f16 v130, v133, 1.0 op_sel:[0,0,1]
	v_pk_fma_f16 v133, v134, v134, -2.0 op_sel:[0,1,1] op_sel_hi:[1,1,0]
	v_mul_f32_e32 v134, 0.15915494, v181
	v_cos_f32_e32 v135, v134
	v_sin_f32_e32 v134, v134
	v_cvt_scalef32_pk_fp8_f16 v132, v133, 1.0
	v_pk_fma_f16 v133, v133, v133, -2.0 op_sel:[0,1,1] op_sel_hi:[1,1,0]
	ds_read_b128 v[170:173], v234 offset:28672
	ds_read_b128 v[174:177], v234 offset:29696
	ds_read_b128 v[236:239], v234 offset:30720
	ds_read_b128 v[240:243], v234 offset:31744
	v_cvt_scalef32_pk_fp8_f16 v132, v133, 1.0 op_sel:[0,0,1]
	v_add_f32_e32 v133, v135, v135
	v_mfma_scale_f32_32x32x64_f8f6f4 v[112:127], v[152:159], v[144:151], v[112:127], v227, v226 op_sel_hi:[0,0,0]
	v_cvt_pk_f16_f32 v152, v134, v133
	v_mul_f32_e32 v153, 0.15915494, v188
	v_lshl_add_u64 v[134:135], v[160:161], 2, s[4:5]
	v_mul_f32_e32 v154, 0.15915494, v189
	global_load_dwordx4 v[178:181], v[134:135], off offset:32
	global_load_dwordx4 v[186:189], v[134:135], off offset:3488
	v_pk_fma_f16 v134, v152, v152, -2.0 op_sel:[1,0,1] op_sel_hi:[1,1,0]
	v_cvt_scalef32_pk_fp8_f16 v133, v152, 1.0
	v_pk_fma_f16 v152, v134, v134, -2.0 op_sel:[0,1,1] op_sel_hi:[1,1,0]
	v_cvt_scalef32_pk_fp8_f16 v133, v134, 1.0 op_sel:[0,0,1]
	v_pk_fma_f16 v155, v152, v152, -2.0 op_sel:[0,1,1] op_sel_hi:[1,1,0]
	v_pk_fma_f16 v134, v155, v155, -2.0 op_sel:[0,1,1] op_sel_hi:[1,1,0]
	v_pk_fma_f16 v156, v134, v134, -2.0 op_sel:[0,1,1] op_sel_hi:[1,1,0]
	v_cvt_scalef32_pk_fp8_f16 v135, v134, 1.0
	v_cvt_scalef32_pk_fp8_f16 v134, v152, 1.0
	v_pk_fma_f16 v152, v203, v203, -2.0 op_sel:[0,1,1] op_sel_hi:[1,1,0]
	v_cvt_scalef32_pk_fp8_f16 v134, v155, 1.0 op_sel:[0,0,1]
	v_pk_fma_f16 v155, v152, v152, -2.0 op_sel:[0,1,1] op_sel_hi:[1,1,0]
	s_waitcnt lgkmcnt(4)
	v_mfma_scale_f32_32x32x64_f8f6f4 v[64:79], v[162:169], v[136:143], v[64:79], v227, v226 op_sel_hi:[0,0,0]
	v_cvt_scalef32_pk_fp8_f16 v135, v156, 1.0 op_sel:[0,0,1]
	v_pk_fma_f16 v156, v155, v155, -2.0 op_sel:[0,1,1] op_sel_hi:[1,1,0]
	v_pk_fma_f16 v157, v156, v156, -2.0 op_sel:[0,1,1] op_sel_hi:[1,1,0]
	v_mfma_scale_f32_32x32x64_f8f6f4 v[80:95], v[162:169], v[144:151], v[80:95], v227, v226 op_sel_hi:[0,0,0]
	v_cvt_scalef32_pk_fp8_f16 v165, v156, 1.0
	v_cos_f32_e32 v156, v153
	v_sin_f32_e32 v153, v153
	v_cvt_scalef32_pk_fp8_f16 v164, v152, 1.0
	v_add_f32_e32 v152, v156, v156
	v_cvt_pk_f16_f32 v152, v153, v152
	v_pk_fma_f16 v153, v152, v152, -2.0 op_sel:[1,0,1] op_sel_hi:[1,1,0]
	v_cvt_scalef32_pk_fp8_f16 v166, v152, 1.0
	v_cvt_scalef32_pk_fp8_f16 v164, v155, 1.0 op_sel:[0,0,1]
	v_pk_fma_f16 v155, v153, v153, -2.0 op_sel:[0,1,1] op_sel_hi:[1,1,0]
	v_cvt_scalef32_pk_fp8_f16 v166, v153, 1.0 op_sel:[0,0,1]
	s_waitcnt lgkmcnt(0)
	v_mfma_scale_f32_32x32x64_f8f6f4 v[0:15], v[236:243], v[136:143], v[0:15], v227, v226 op_sel_hi:[0,0,0]
	v_cos_f32_e32 v153, v154
	v_cvt_scalef32_pk_fp8_f16 v167, v155, 1.0
	v_pk_fma_f16 v155, v155, v155, -2.0 op_sel:[0,1,1] op_sel_hi:[1,1,0]
	v_sin_f32_e32 v154, v154
	v_pk_fma_f16 v152, v155, v155, -2.0 op_sel:[0,1,1] op_sel_hi:[1,1,0]
	v_cvt_scalef32_pk_fp8_f16 v168, v152, 1.0
	v_pk_fma_f16 v152, v152, v152, -2.0 op_sel:[0,1,1] op_sel_hi:[1,1,0]
	v_cvt_scalef32_pk_fp8_f16 v168, v152, 1.0 op_sel:[0,0,1]
	v_add_f32_e32 v152, v153, v153
	v_cvt_scalef32_pk_fp8_f16 v165, v157, 1.0 op_sel:[0,0,1]
	v_cvt_scalef32_pk_fp8_f16 v167, v155, 1.0 op_sel:[0,0,1]
	v_mfma_scale_f32_32x32x64_f8f6f4 v[32:47], v[170:177], v[136:143], v[32:47], v227, v226 op_sel_hi:[0,0,0]
	v_cvt_pk_f16_f32 v136, v154, v152
	v_cvt_scalef32_pk_fp8_f16 v169, v136, 1.0
	v_pk_fma_f16 v136, v136, v136, -2.0 op_sel:[1,0,1] op_sel_hi:[1,1,0]
	v_cvt_scalef32_pk_fp8_f16 v169, v136, 1.0 op_sel:[0,0,1]
	v_pk_fma_f16 v136, v136, v136, -2.0 op_sel:[0,1,1] op_sel_hi:[1,1,0]
	v_pk_fma_f16 v137, v136, v136, -2.0 op_sel:[0,1,1] op_sel_hi:[1,1,0]
	v_pk_fma_f16 v138, v137, v137, -2.0 op_sel:[0,1,1] op_sel_hi:[1,1,0]
	v_pk_fma_f16 v139, v138, v138, -2.0 op_sel:[0,1,1] op_sel_hi:[1,1,0]
	v_mfma_scale_f32_32x32x64_f8f6f4 v[48:63], v[170:177], v[144:151], v[48:63], v227, v226 op_sel_hi:[0,0,0]
	v_cvt_scalef32_pk_fp8_f16 v171, v138, 1.0
	v_cvt_scalef32_pk_fp8_f16 v170, v136, 1.0
	v_cvt_scalef32_pk_fp8_f16 v171, v139, 1.0 op_sel:[0,0,1]
	v_cvt_scalef32_pk_fp8_f16 v170, v137, 1.0 op_sel:[0,0,1]
	v_mfma_scale_f32_32x32x64_f8f6f4 v[16:31], v[236:243], v[144:151], v[16:31], v227, v226 op_sel_hi:[0,0,0]
	v_mul_f32_e32 v152, 0.15915494, v225
	ds_read_b128 v[136:139], v234 offset:32768
	ds_read_b128 v[140:143], v234 offset:33792
	v_cos_f32_e32 v153, v152
	v_sin_f32_e32 v152, v152
	v_mov_b32_e32 v205, v161
	s_waitcnt lgkmcnt(0)
	v_mfma_scale_f32_32x32x64_f8f6f4 v[96:111], v[136:143], v[128:135], v[96:111], v227, v226 op_sel_hi:[0,0,0]
	v_add_f32_e32 v153, v153, v153
	v_cvt_pk_f16_f32 v158, v152, v153
	v_mov_b32_e32 v203, v161
	v_cndmask_b32_e64 v162, 0, v222, s[0:1]
	v_mul_f32_e32 v163, 0.15915494, v223
	v_pk_fma_f16 v159, v158, v158, -2.0 op_sel:[1,0,1] op_sel_hi:[1,1,0]
	v_cndmask_b32_e64 v172, 0, v224, s[0:1]
	v_pk_fma_f16 v156, v159, v159, -2.0 op_sel:[0,1,1] op_sel_hi:[1,1,0]
	v_pk_fma_f16 v160, v156, v156, -2.0 op_sel:[0,1,1] op_sel_hi:[1,1,0]
	v_cvt_scalef32_pk_fp8_f16 v157, v156, 1.0
	v_cvt_scalef32_pk_fp8_f16 v156, v158, 1.0
	v_cvt_scalef32_pk_fp8_f16 v156, v159, 1.0 op_sel:[0,0,1]
	v_mfma_scale_f32_32x32x64_f8f6f4 v[112:127], v[136:143], v[164:171], v[112:127], v227, v226 op_sel_hi:[0,0,0]
	ds_read_b128 v[136:139], v234 offset:34816
	ds_read_b128 v[140:143], v234 offset:35840
	ds_read_b128 v[144:147], v234 offset:36864
	ds_read_b128 v[148:151], v234 offset:37888
	ds_read_b128 v[236:239], v234 offset:38912
	ds_read_b128 v[240:243], v234 offset:39936
	v_lshl_add_u64 v[152:153], v[204:205], 2, s[4:5]
	v_lshl_add_u64 v[154:155], v[202:203], 2, s[4:5]
	global_load_dword v225, v[152:153], off offset:48
	global_load_dword v222, v[154:155], off
	global_load_dword v224, v[154:155], off offset:3456
	global_load_dword v223, v[152:153], off offset:3504
	v_cvt_scalef32_pk_fp8_f16 v157, v160, 1.0 op_sel:[0,0,1]
	s_waitcnt lgkmcnt(4)
	v_mfma_scale_f32_32x32x64_f8f6f4 v[64:79], v[136:143], v[128:135], v[64:79], v227, v226 op_sel_hi:[0,0,0]
	v_mfma_scale_f32_32x32x64_f8f6f4 v[80:95], v[136:143], v[164:171], v[80:95], v227, v226 op_sel_hi:[0,0,0]
	v_mul_f32_e32 v136, v207, v208
	v_fma_f32 v137, v208, v208, -2.0
	v_cndmask_b32_e64 v138, v137, v136, s[0:1]
	v_mul_f32_e32 v136, v136, v137
	v_fma_f32 v137, v137, v137, -2.0
	v_cndmask_b32_e64 v139, v137, v136, s[0:1]
	v_cvt_pk_fp8_f32 v159, v138, v139
	v_mul_f32_e32 v136, v136, v137
	v_fma_f32 v137, v137, v137, -2.0
	v_cndmask_b32_e64 v136, v137, v136, s[0:1]
	v_cvt_pk_fp8_f32 v159, v136, v162 op_sel:[0,0,1]
	v_pk_fma_f16 v136, v160, v160, -2.0 op_sel:[0,1,1] op_sel_hi:[1,1,0]
	v_mov_b32_e32 v160, v161
	v_pk_fma_f16 v137, v136, v136, -2.0 op_sel:[0,1,1] op_sel_hi:[1,1,0]
	v_cvt_scalef32_pk_fp8_f16 v158, v136, 1.0
	v_cos_f32_e32 v136, v163
	v_cvt_scalef32_pk_fp8_f16 v158, v137, 1.0 op_sel:[0,0,1]
	v_sin_f32_e32 v137, v163
	s_waitcnt lgkmcnt(0)
	v_mfma_scale_f32_32x32x64_f8f6f4 v[0:15], v[236:243], v[128:135], v[0:15], v227, v226 op_sel_hi:[0,0,0]
	v_add_f32_e32 v136, v136, v136
	v_mov_b32_e32 v162, v161
	v_cvt_pk_f16_f32 v138, v137, v136
	v_pk_fma_f16 v139, v138, v138, -2.0 op_sel:[1,0,1] op_sel_hi:[1,1,0]
	v_pk_fma_f16 v136, v139, v139, -2.0 op_sel:[0,1,1] op_sel_hi:[1,1,0]
	v_mov_b32_e32 v163, v161
	v_pk_fma_f16 v140, v136, v136, -2.0 op_sel:[0,1,1] op_sel_hi:[1,1,0]
	v_cvt_scalef32_pk_fp8_f16 v137, v136, 1.0
	v_cvt_scalef32_pk_fp8_f16 v136, v138, 1.0
	v_cvt_scalef32_pk_fp8_f16 v136, v139, 1.0 op_sel:[0,0,1]
	v_mul_f32_e32 v138, v209, v210
	v_fma_f32 v139, v210, v210, -2.0
	v_cndmask_b32_e64 v141, v139, v138, s[0:1]
	v_mul_f32_e32 v138, v138, v139
	v_fma_f32 v142, v139, v139, -2.0
	v_cndmask_b32_e64 v143, v142, v138, s[0:1]
	v_cvt_pk_fp8_f32 v139, v141, v143
	v_mfma_scale_f32_32x32x64_f8f6f4 v[32:47], v[144:151], v[128:135], v[32:47], v227, v226 op_sel_hi:[0,0,0]
	v_mul_f32_e32 v128, v138, v142
	v_fma_f32 v129, v142, v142, -2.0
	v_cndmask_b32_e64 v128, v129, v128, s[0:1]
	v_cvt_pk_fp8_f32 v139, v128, v172 op_sel:[0,0,1]
	v_pk_fma_f16 v128, v140, v140, -2.0 op_sel:[0,1,1] op_sel_hi:[1,1,0]
	v_cvt_scalef32_pk_fp8_f16 v138, v128, 1.0
	v_pk_fma_f16 v128, v128, v128, -2.0 op_sel:[0,1,1] op_sel_hi:[1,1,0]
	v_cvt_scalef32_pk_fp8_f16 v137, v140, 1.0 op_sel:[0,0,1]
	v_cvt_scalef32_pk_fp8_f16 v138, v128, 1.0 op_sel:[0,0,1]
	v_mov_b32_e32 v140, v161
	v_mov_b32_e32 v141, v161
	v_mov_b32_e32 v142, v161
	v_mov_b32_e32 v143, v161
	v_mfma_scale_f32_32x32x64_f8f6f4 v[48:63], v[144:151], v[164:171], v[48:63], v227, v226 op_sel_hi:[0,0,0]
	v_mfma_scale_f32_32x32x64_f8f6f4 v[16:31], v[236:243], v[164:171], v[16:31], v227, v226 op_sel_hi:[0,0,0]
	ds_read_b128 v[128:131], v234 offset:40960
	ds_read_b128 v[132:135], v234 offset:41984
	s_waitcnt lgkmcnt(0)
	v_mfma_scale_f32_32x32x64_f8f6f4 v[96:111], v[128:135], v[156:163], v[96:111], v227, v226 op_sel_hi:[0,0,0]
	v_mfma_scale_f32_32x32x64_f8f6f4 v[112:127], v[128:135], v[136:143], v[112:127], v227, v226 op_sel_hi:[0,0,0]
	ds_read_b128 v[128:131], v234 offset:43008
	ds_read_b128 v[132:135], v234 offset:44032
	s_waitcnt lgkmcnt(0)
	v_mfma_scale_f32_32x32x64_f8f6f4 v[64:79], v[128:135], v[156:163], v[64:79], v227, v226 op_sel_hi:[0,0,0]
	v_mfma_scale_f32_32x32x64_f8f6f4 v[80:95], v[128:135], v[136:143], v[80:95], v227, v226 op_sel_hi:[0,0,0]
	ds_read_b128 v[128:131], v234 offset:45056
	ds_read_b128 v[132:135], v234 offset:46080
	s_waitcnt lgkmcnt(0)
	v_mfma_scale_f32_32x32x64_f8f6f4 v[32:47], v[128:135], v[156:163], v[32:47], v227, v226 op_sel_hi:[0,0,0]
	v_mfma_scale_f32_32x32x64_f8f6f4 v[48:63], v[128:135], v[136:143], v[48:63], v227, v226 op_sel_hi:[0,0,0]
	ds_read_b128 v[128:131], v234 offset:47104
	ds_read_b128 v[132:135], v234 offset:48128
	ds_read_b128 v[174:177], v234 offset:49152
	ds_read_b128 v[208:211], v234 offset:50176
	ds_read_b128 v[212:215], v234 offset:53248
	ds_read_b128 v[236:239], v234 offset:54272
	s_waitcnt lgkmcnt(4)
	v_mfma_scale_f32_32x32x64_f8f6f4 v[0:15], v[128:135], v[156:163], v[0:15], v227, v226 op_sel_hi:[0,0,0]
	v_mfma_scale_f32_32x32x64_f8f6f4 v[16:31], v[128:135], v[136:143], v[16:31], v227, v226 op_sel_hi:[0,0,0]
	v_cvt_pk_bf16_f32 v162, v96, v97 clamp
	v_cvt_pk_bf16_f32 v163, v98, v99 clamp
	v_cvt_pk_bf16_f32 v164, v100, v101 clamp
	v_cvt_pk_bf16_f32 v165, v102, v103 clamp
	v_cvt_pk_bf16_f32 v166, v112, v113 clamp
	v_cvt_pk_bf16_f32 v167, v114, v115 clamp
	v_cvt_pk_bf16_f32 v168, v116, v117 clamp
	v_cvt_pk_bf16_f32 v169, v118, v119 clamp
	v_cvt_pk_bf16_f32 v170, v104, v105 clamp
	v_cvt_pk_bf16_f32 v171, v106, v107 clamp
	v_cvt_pk_bf16_f32 v172, v108, v109 clamp
	v_add_u32_e32 v128, 0, v206
	v_cvt_pk_bf16_f32 v173, v110, v111 clamp
	v_add_u32_e32 v235, 0x18000, v128
	v_cvt_pk_bf16_f32 v202, v120, v121 clamp
	ds_read_b128 v[128:131], v235
	ds_read_b128 v[132:135], v235 offset:32
	ds_read_b128 v[136:139], v235 offset:64
	ds_read_b128 v[140:143], v235 offset:96
	v_cvt_pk_bf16_f32 v203, v122, v123 clamp
	ds_read_b128 v[96:99], v235 offset:128
	ds_read_b128 v[100:103], v235 offset:160
	ds_read_b128 v[104:107], v235 offset:192
	ds_read_b128 v[108:111], v235 offset:224
	v_cvt_pk_bf16_f32 v204, v124, v125 clamp
	v_cvt_pk_bf16_f32 v64, v64, v65
	s_waitcnt lgkmcnt(4)
	v_mfma_f32_32x32x16_bf16 v[144:159], v[174:177], v[166:169], v[128:143]
	v_cvt_pk_bf16_f32 v205, v126, v127 clamp
	ds_read_b128 v[240:243], v234 offset:57344
	ds_read_b128 v[244:247], v234 offset:58368
	ds_read_b128 v[248:251], v234 offset:61440
	ds_read_b128 v[252:255], v234 offset:62464
	v_cvt_pk_bf16_f32 v65, v74, v75 clamp
	v_cndmask_b32_e64 v230, v230, 0, s[14:15]
	v_mfma_f32_32x32x16_bf16 v[128:143], v[174:177], v[162:165], v[128:143]
	v_pk_max_i16 v174, v64, 0
	v_cvt_pk_bf16_f32 v175, v66, v67 clamp
	v_cvt_pk_bf16_f32 v176, v68, v69 clamp
	v_cvt_pk_bf16_f32 v177, v70, v71 clamp
	s_waitcnt lgkmcnt(4)
	v_mfma_f32_32x32x16_bf16 v[112:127], v[208:211], v[166:169], v[96:111]
	v_cvt_pk_bf16_f32 v80, v80, v81 clamp
	v_cvt_pk_bf16_f32 v81, v82, v83 clamp
	v_cvt_pk_bf16_f32 v82, v84, v85 clamp
	v_cvt_pk_bf16_f32 v83, v86, v87 clamp
	v_mfma_f32_32x32x16_bf16 v[96:111], v[208:211], v[162:165], v[96:111]
	v_cvt_pk_bf16_f32 v64, v72, v73 clamp
	v_cvt_pk_bf16_f32 v66, v76, v77 clamp
	v_cvt_pk_bf16_f32 v67, v78, v79 clamp
	v_cvt_pk_bf16_f32 v68, v88, v89 clamp
	v_cvt_pk_bf16_f32 v69, v90, v91 clamp
	v_cvt_pk_bf16_f32 v70, v92, v93 clamp
	v_cvt_pk_bf16_f32 v71, v94, v95 clamp
	v_add_u32_e32 v160, 0x14000, v234
	v_mfma_f32_32x32x16_bf16 v[128:143], v[212:215], v[170:173], v[128:143]
	v_mfma_f32_32x32x16_bf16 v[144:159], v[212:215], v[202:205], v[144:159]
	v_mfma_f32_32x32x16_bf16 v[96:111], v[236:239], v[170:173], v[96:111]
	v_mfma_f32_32x32x16_bf16 v[112:127], v[236:239], v[202:205], v[112:127]
	v_cvt_pk_bf16_f32 v76, v32, v33 clamp
	v_cvt_pk_bf16_f32 v77, v34, v35 clamp
	v_cvt_pk_bf16_f32 v78, v36, v37 clamp
	v_cvt_pk_bf16_f32 v79, v38, v39 clamp
	v_cvt_pk_bf16_f32 v88, v48, v49 clamp
	v_cvt_pk_bf16_f32 v89, v50, v51 clamp
	v_cvt_pk_bf16_f32 v90, v52, v53 clamp
	v_cvt_pk_bf16_f32 v91, v54, v55 clamp
	s_waitcnt lgkmcnt(3)
	v_mfma_f32_32x32x16_bf16 v[128:143], v[240:243], v[174:177], v[128:143]
	v_cvt_pk_bf16_f32 v72, v40, v41 clamp
	v_cvt_pk_bf16_f32 v73, v42, v43 clamp
	v_cvt_pk_bf16_f32 v74, v44, v45 clamp
	v_mfma_f32_32x32x16_bf16 v[144:159], v[240:243], v[80:83], v[144:159]
	ds_read_b128 v[92:95], v233 offset:16384
	ds_read_b128 v[208:211], v233 offset:17408
	ds_read_b128 v[236:239], v233 offset:20480
	ds_read_b128 v[240:243], v233 offset:21504
	v_cvt_pk_bf16_f32 v75, v46, v47 clamp
	v_cvt_pk_bf16_f32 v84, v56, v57 clamp
	v_cvt_pk_bf16_f32 v85, v58, v59 clamp
	s_waitcnt lgkmcnt(6)
	v_mfma_f32_32x32x16_bf16 v[96:111], v[244:247], v[174:177], v[96:111]
	v_cvt_pk_bf16_f32 v86, v60, v61 clamp
	v_cvt_pk_bf16_f32 v87, v62, v63 clamp
	v_mfma_f32_32x32x16_bf16 v[112:127], v[244:247], v[80:83], v[112:127]
	s_waitcnt lgkmcnt(5)
	v_mfma_f32_32x32x16_bf16 v[128:143], v[248:251], v[64:67], v[128:143]
	v_mfma_f32_32x32x16_bf16 v[144:159], v[248:251], v[68:71], v[144:159]
	s_waitcnt lgkmcnt(4)
	v_mfma_f32_32x32x16_bf16 v[96:111], v[252:255], v[64:67], v[96:111]
	v_mfma_f32_32x32x16_bf16 v[112:127], v[252:255], v[68:71], v[112:127]
	v_cvt_pk_bf16_f32 v206, v0, v1 clamp
	v_cvt_pk_bf16_f32 v207, v2, v3 clamp
	v_cvt_pk_bf16_f32 v0, v4, v5
	s_waitcnt lgkmcnt(2)
	v_mfma_f32_32x32x16_bf16 v[96:111], v[208:211], v[76:79], v[96:111]
	ds_read_b128 v[32:35], v233 offset:24576
	ds_read_b128 v[36:39], v233 offset:25600
	ds_read_b128 v[40:43], v233 offset:28672
	ds_read_b128 v[44:47], v233 offset:29696
	v_mfma_f32_32x32x16_bf16 v[112:127], v[208:211], v[88:91], v[112:127]
	v_pk_max_i16 v208, v0, 0
	v_cvt_pk_bf16_f32 v209, v6, v7 clamp
	v_cvt_pk_bf16_f32 v214, v16, v17 clamp
	v_cvt_pk_bf16_f32 v215, v18, v19 clamp
	v_cvt_pk_bf16_f32 v216, v20, v21 clamp
	v_cvt_pk_bf16_f32 v217, v22, v23 clamp
	v_mfma_f32_32x32x16_bf16 v[128:143], v[92:95], v[76:79], v[128:143]
	v_cvt_pk_bf16_f32 v0, v8, v9
	v_mfma_f32_32x32x16_bf16 v[144:159], v[92:95], v[88:91], v[144:159]
	v_pk_max_i16 v92, v0, 0
	v_cvt_pk_bf16_f32 v93, v10, v11 clamp
	v_cvt_pk_bf16_f32 v94, v12, v13 clamp
	v_cvt_pk_bf16_f32 v95, v14, v15 clamp
	v_cvt_pk_bf16_f32 v210, v24, v25 clamp
	v_cvt_pk_bf16_f32 v211, v26, v27 clamp
	v_cvt_pk_bf16_f32 v212, v28, v29 clamp
	v_cvt_pk_bf16_f32 v213, v30, v31 clamp
	s_waitcnt lgkmcnt(5)
	v_mfma_f32_32x32x16_bf16 v[128:143], v[236:239], v[72:75], v[128:143]
	v_mfma_f32_32x32x16_bf16 v[144:159], v[236:239], v[84:87], v[144:159]
	s_waitcnt lgkmcnt(4)
	v_mfma_f32_32x32x16_bf16 v[96:111], v[240:243], v[72:75], v[96:111]
	v_mfma_f32_32x32x16_bf16 v[112:127], v[240:243], v[84:87], v[112:127]
	s_waitcnt lgkmcnt(3)
	v_mfma_f32_32x32x16_bf16 v[128:143], v[32:35], v[206:209], v[128:143]
	ds_read_b128 v[0:3], v234 offset:51200
	ds_read_b128 v[236:239], v234 offset:52224
	ds_read_b128 v[240:243], v234 offset:55296
	ds_read_b128 v[244:247], v234 offset:56320
	v_mfma_f32_32x32x16_bf16 v[144:159], v[32:35], v[214:217], v[144:159]
	s_waitcnt lgkmcnt(6)
	v_mfma_f32_32x32x16_bf16 v[96:111], v[36:39], v[206:209], v[96:111]
	v_mfma_f32_32x32x16_bf16 v[112:127], v[36:39], v[214:217], v[112:127]
	s_waitcnt lgkmcnt(5)
	v_mfma_f32_32x32x16_bf16 v[128:143], v[40:43], v[92:95], v[128:143]
	v_mfma_f32_32x32x16_bf16 v[144:159], v[40:43], v[210:213], v[144:159]
	s_waitcnt lgkmcnt(4)
	v_mfma_f32_32x32x16_bf16 v[96:111], v[44:47], v[92:95], v[96:111]
	v_mfma_f32_32x32x16_bf16 v[112:127], v[44:47], v[210:213], v[112:127]
	ds_read_b128 v[32:35], v235 offset:256
	ds_read_b128 v[36:39], v235 offset:288
	ds_read_b128 v[40:43], v235 offset:320
	ds_read_b128 v[44:47], v235 offset:352
	s_nop 3
	v_cvt_pk_bf16_f32 v128, v128, v129 clamp
	v_cvt_pk_bf16_f32 v129, v130, v131 clamp
	v_cvt_pk_bf16_f32 v130, v132, v133 clamp
	v_cvt_pk_bf16_f32 v131, v134, v135 clamp
	s_waitcnt lgkmcnt(0)
	v_mfma_f32_32x32x16_bf16 v[48:63], v[0:3], v[166:169], v[32:47]
	v_cvt_pk_bf16_f32 v132, v144, v145 clamp
	v_cvt_pk_bf16_f32 v133, v146, v147 clamp
	v_cvt_pk_bf16_f32 v134, v148, v149 clamp
	v_cvt_pk_bf16_f32 v135, v150, v151 clamp
	v_mfma_f32_32x32x16_bf16 v[32:47], v[0:3], v[162:165], v[32:47]
	ds_read_b128 v[0:3], v235 offset:384
	ds_read_b128 v[4:7], v235 offset:416
	ds_read_b128 v[8:11], v235 offset:448
	ds_read_b128 v[12:15], v235 offset:480
	s_waitcnt lgkmcnt(0)
	v_mfma_f32_32x32x16_bf16 v[16:31], v[236:239], v[166:169], v[0:15]
	v_mfma_f32_32x32x16_bf16 v[0:15], v[236:239], v[162:165], v[0:15]
	ds_read_b128 v[162:165], v234 offset:59392
	ds_read_b128 v[166:169], v234 offset:60416
	ds_read_b128 v[236:239], v234 offset:63488
	ds_read_b128 v[248:251], v234 offset:64512
	v_mfma_f32_32x32x16_bf16 v[0:15], v[244:247], v[170:173], v[0:15]
	v_mfma_f32_32x32x16_bf16 v[32:47], v[240:243], v[170:173], v[32:47]
	v_mfma_f32_32x32x16_bf16 v[48:63], v[240:243], v[202:205], v[48:63]
	v_mfma_f32_32x32x16_bf16 v[16:31], v[244:247], v[202:205], v[16:31]
	s_waitcnt lgkmcnt(2)
	v_mfma_f32_32x32x16_bf16 v[0:15], v[166:169], v[174:177], v[0:15]
	v_cvt_pk_bf16_f32 v136, v136, v137 clamp
	v_cvt_pk_bf16_f32 v137, v138, v139 clamp
	v_cvt_pk_bf16_f32 v138, v140, v141 clamp
	v_cvt_pk_bf16_f32 v139, v142, v143 clamp
	v_cvt_pk_bf16_f32 v140, v152, v153 clamp
	v_mfma_f32_32x32x16_bf16 v[32:47], v[162:165], v[174:177], v[32:47]
	v_mfma_f32_32x32x16_bf16 v[48:63], v[162:165], v[80:83], v[48:63]
	v_mfma_f32_32x32x16_bf16 v[16:31], v[166:169], v[80:83], v[16:31]
	ds_read_b128 v[80:83], v233 offset:18432
	ds_read_b128 v[144:147], v233 offset:19456
	ds_read_b128 v[148:151], v233 offset:22528
	ds_read_b128 v[162:165], v233 offset:23552
	s_waitcnt lgkmcnt(4)
	v_mfma_f32_32x32x16_bf16 v[0:15], v[248:251], v[64:67], v[0:15]
	v_mfma_f32_32x32x16_bf16 v[32:47], v[236:239], v[64:67], v[32:47]
	v_cvt_pk_bf16_f32 v141, v154, v155 clamp
	v_cvt_pk_bf16_f32 v142, v156, v157 clamp
	v_cvt_pk_bf16_f32 v143, v158, v159 clamp
	v_mfma_f32_32x32x16_bf16 v[48:63], v[236:239], v[68:71], v[48:63]
	v_mfma_f32_32x32x16_bf16 v[16:31], v[248:251], v[68:71], v[16:31]
	s_waitcnt lgkmcnt(2)
	v_mfma_f32_32x32x16_bf16 v[0:15], v[144:147], v[76:79], v[0:15]
	v_mfma_f32_32x32x16_bf16 v[32:47], v[80:83], v[76:79], v[32:47]
	v_mfma_f32_32x32x16_bf16 v[48:63], v[80:83], v[88:91], v[48:63]
	ds_read_b128 v[64:67], v233 offset:26624
	ds_read_b128 v[68:71], v233 offset:27648
	ds_read_b128 v[76:79], v233 offset:30720
	ds_read_b128 v[80:83], v233 offset:31744
	v_mfma_f32_32x32x16_bf16 v[16:31], v[144:147], v[88:91], v[16:31]
	v_cvt_pk_bf16_f32 v96, v96, v97 clamp
	v_cvt_pk_bf16_f32 v97, v98, v99 clamp
	v_cvt_pk_bf16_f32 v98, v100, v101 clamp
	v_cvt_pk_bf16_f32 v99, v102, v103 clamp
	s_waitcnt lgkmcnt(4)
	v_mfma_f32_32x32x16_bf16 v[0:15], v[162:165], v[72:75], v[0:15]
	v_cvt_pk_bf16_f32 v100, v112, v113 clamp
	v_mfma_f32_32x32x16_bf16 v[32:47], v[148:151], v[72:75], v[32:47]
	v_cvt_pk_bf16_f32 v101, v114, v115 clamp
	v_cvt_pk_bf16_f32 v102, v116, v117 clamp
	v_cvt_pk_bf16_f32 v103, v118, v119 clamp
	v_mfma_f32_32x32x16_bf16 v[48:63], v[148:151], v[84:87], v[48:63]
	v_mfma_f32_32x32x16_bf16 v[16:31], v[162:165], v[84:87], v[16:31]
	s_waitcnt lgkmcnt(2)
	v_mfma_f32_32x32x16_bf16 v[0:15], v[68:71], v[206:209], v[0:15]
	ds_read_b128 v[84:87], v160
	ds_read_b128 v[112:115], v160 offset:1024
	ds_read_b128 v[116:119], v160 offset:2048
	ds_read_b128 v[144:147], v160 offset:3072
	v_mfma_f32_32x32x16_bf16 v[32:47], v[64:67], v[206:209], v[32:47]
	v_mfma_f32_32x32x16_bf16 v[48:63], v[64:67], v[214:217], v[48:63]
	v_cvt_pk_bf16_f32 v104, v104, v105 clamp
	v_cvt_pk_bf16_f32 v105, v106, v107 clamp
	v_cvt_pk_bf16_f32 v106, v108, v109 clamp
	v_cvt_pk_bf16_f32 v107, v110, v111 clamp
	v_mfma_f32_32x32x16_bf16 v[16:31], v[68:71], v[214:217], v[16:31]
	v_cvt_pk_bf16_f32 v108, v120, v121 clamp
	v_cvt_pk_bf16_f32 v109, v122, v123 clamp
	v_cvt_pk_bf16_f32 v110, v124, v125 clamp
	s_waitcnt lgkmcnt(4)
	v_mfma_f32_32x32x16_bf16 v[0:15], v[80:83], v[92:95], v[0:15]
	v_cvt_pk_bf16_f32 v111, v126, v127 clamp
	v_mfma_f32_32x32x16_bf16 v[32:47], v[76:79], v[92:95], v[32:47]
	v_mfma_f32_32x32x16_bf16 v[48:63], v[76:79], v[210:213], v[48:63]
	v_mfma_f32_32x32x16_bf16 v[16:31], v[80:83], v[210:213], v[16:31]
	s_waitcnt lgkmcnt(3)
	v_mfma_f32_4x4x4_16b_bf16 v[64:67], v[84:85], v[128:129], 0
	v_mfma_f32_4x4x4_16b_bf16 v[68:71], v[86:87], v[130:131], 0
	s_nop 7
	v_cvt_pk_bf16_f32 v32, v32, v33 clamp
	v_cvt_pk_bf16_f32 v33, v34, v35 clamp
	v_cvt_pk_bf16_f32 v34, v36, v37 clamp
	v_cvt_pk_bf16_f32 v35, v38, v39 clamp
	v_mfma_f32_4x4x4_16b_bf16 v[80:83], v[84:85], v[132:133], 0
	v_mfma_f32_4x4x4_16b_bf16 v[88:91], v[86:87], v[134:135], 0
	v_cvt_pk_bf16_f32 v48, v48, v49 clamp
	v_cvt_pk_bf16_f32 v49, v50, v51 clamp
	v_cvt_pk_bf16_f32 v50, v52, v53 clamp
	v_cvt_pk_bf16_f32 v51, v54, v55 clamp
	s_waitcnt lgkmcnt(2)
	v_mfma_f32_4x4x4_16b_bf16 v[64:67], v[112:113], v[136:137], v[64:67]
	v_mfma_f32_4x4x4_16b_bf16 v[68:71], v[114:115], v[138:139], v[68:71]
	v_cvt_pk_bf16_f32 v40, v40, v41 clamp
	v_cvt_pk_bf16_f32 v41, v42, v43 clamp
	v_cvt_pk_bf16_f32 v42, v44, v45 clamp
	v_cvt_pk_bf16_f32 v43, v46, v47 clamp
	v_mfma_f32_4x4x4_16b_bf16 v[80:83], v[112:113], v[140:141], v[80:83]
	v_mfma_f32_4x4x4_16b_bf16 v[88:91], v[114:115], v[142:143], v[88:91]
	v_cvt_pk_bf16_f32 v52, v56, v57
	v_cvt_pk_bf16_f32 v53, v58, v59
	v_cvt_pk_bf16_f32 v54, v60, v61
	v_cvt_pk_bf16_f32 v55, v62, v63
	s_waitcnt lgkmcnt(1)
	v_mfma_f32_4x4x4_16b_bf16 v[64:67], v[116:117], v[96:97], v[64:67]
	v_mfma_f32_4x4x4_16b_bf16 v[68:71], v[118:119], v[98:99], v[68:71]
	ds_read_b128 v[36:39], v160 offset:4096
	ds_read_b128 v[96:99], v160 offset:5120
	v_cvt_pk_bf16_f32 v0, v0, v1 clamp
	v_cvt_pk_bf16_f32 v1, v2, v3 clamp
	v_cvt_pk_bf16_f32 v2, v4, v5 clamp
	v_cvt_pk_bf16_f32 v3, v6, v7 clamp
	v_mfma_f32_4x4x4_16b_bf16 v[80:83], v[116:117], v[100:101], v[80:83]
	v_mfma_f32_4x4x4_16b_bf16 v[88:91], v[118:119], v[102:103], v[88:91]
	ds_read_b128 v[4:7], v160 offset:7168
	v_cvt_pk_bf16_f32 v12, v12, v13
	v_cvt_pk_bf16_f32 v13, v14, v15
	v_cvt_pk_bf16_f32 v24, v24, v25
	v_cvt_pk_bf16_f32 v25, v26, v27
	s_waitcnt lgkmcnt(3)
	v_mfma_f32_4x4x4_16b_bf16 v[64:67], v[144:145], v[104:105], v[64:67]
	v_mfma_f32_4x4x4_16b_bf16 v[68:71], v[146:147], v[106:107], v[68:71]
	v_cvt_pk_bf16_f32 v26, v28, v29
	v_cvt_pk_bf16_f32 v27, v30, v31
	v_cndmask_b32_e64 v219, v219, 0, s[14:15]
	v_cndmask_b32_e64 v218, v218, 0, s[14:15]
	v_mfma_f32_4x4x4_16b_bf16 v[80:83], v[144:145], v[108:109], v[80:83]
	v_mfma_f32_4x4x4_16b_bf16 v[88:91], v[146:147], v[110:111], v[88:91]
	s_waitcnt lgkmcnt(2)
	v_mfma_f32_4x4x4_16b_bf16 v[64:67], v[36:37], v[32:33], v[64:67]
	v_mfma_f32_4x4x4_16b_bf16 v[68:71], v[38:39], v[34:35], v[68:71]
	v_cvt_pk_bf16_f32 v34, v20, v21
	v_cvt_pk_bf16_f32 v35, v22, v23
	ds_read_b128 v[20:23], v160 offset:6144
	v_cvt_pk_bf16_f32 v32, v16, v17
	v_cvt_pk_bf16_f32 v33, v18, v19
	v_pk_max_i16 v16, v52, 0
	v_pk_max_i16 v17, v53, 0
	v_mfma_f32_4x4x4_16b_bf16 v[80:83], v[36:37], v[48:49], v[80:83]
	v_mfma_f32_4x4x4_16b_bf16 v[88:91], v[38:39], v[50:51], v[88:91]
	v_pk_max_i16 v18, v54, 0
	v_pk_max_i16 v19, v55, 0
	s_waitcnt lgkmcnt(2)
	v_mfma_f32_4x4x4_16b_bf16 v[64:67], v[96:97], v[40:41], v[64:67]
	v_mfma_f32_4x4x4_16b_bf16 v[68:71], v[98:99], v[42:43], v[68:71]
	v_mfma_f32_4x4x4_16b_bf16 v[80:83], v[96:97], v[16:17], v[80:83]
	v_mfma_f32_4x4x4_16b_bf16 v[88:91], v[98:99], v[18:19], v[88:91]
	v_cvt_pk_bf16_f32 v16, v8, v9
	v_cvt_pk_bf16_f32 v17, v10, v11
	v_pk_max_i16 v8, v24, 0
	v_pk_max_i16 v9, v25, 0
	v_pk_max_i16 v10, v26, 0
	v_pk_max_i16 v11, v27, 0
	s_waitcnt lgkmcnt(0)
	v_mfma_f32_4x4x4_16b_bf16 v[64:67], v[20:21], v[0:1], v[64:67]
	v_mfma_f32_4x4x4_16b_bf16 v[68:71], v[22:23], v[2:3], v[68:71]
	v_pk_max_i16 v0, v32, 0
	v_pk_max_i16 v1, v33, 0
	v_pk_max_i16 v2, v34, 0
	v_pk_max_i16 v3, v35, 0
	s_nop 1
	v_mfma_f32_4x4x4_16b_bf16 v[80:83], v[20:21], v[0:1], v[80:83]
	v_mfma_f32_4x4x4_16b_bf16 v[88:91], v[22:23], v[2:3], v[88:91]
	v_pk_max_i16 v0, v16, 0
	v_pk_max_i16 v1, v17, 0
	v_pk_max_i16 v2, v12, 0
	v_pk_max_i16 v3, v13, 0
	s_nop 1
	v_mfma_f32_4x4x4_16b_bf16 v[64:67], v[4:5], v[0:1], v[64:67]
	v_mfma_f32_4x4x4_16b_bf16 v[68:71], v[6:7], v[2:3], v[68:71]
	v_mfma_f32_4x4x4_16b_bf16 v[80:83], v[4:5], v[8:9], v[80:83]
	v_mfma_f32_4x4x4_16b_bf16 v[88:91], v[6:7], v[10:11], v[88:91]
	s_waitcnt vmcnt(10)
	s_nop 3
	v_pk_add_f32 v[64:65], v[64:65], v[68:69]
	v_pk_add_f32 v[80:81], v[80:81], v[88:89]
	v_add_f32_e32 v66, v66, v70
	v_add_f32_e32 v82, v82, v90
	s_nop 1
	v_permlane32_swap_b32_e32 v64, v80
	v_permlane32_swap_b32_e32 v65, v81
	v_permlane32_swap_b32_e32 v66, v82
	s_nop 0
	v_add_f32_e32 v64, v64, v80
	v_add_f32_e32 v65, v65, v81
	v_add_f32_e32 v66, v66, v82
	v_add_f32_e32 v3, s10, v64
	v_add_f32_e32 v4, s11, v65
	v_add_f32_e32 v5, s18, v66
	v_mul_f32_e32 v3, 0xbfb8aa3b, v3
	v_mul_f32_e32 v4, 0xbfb8aa3b, v4
	v_mul_f32_e32 v5, 0xbfb8aa3b, v5
	v_exp_f32_e32 v3, v3
	v_exp_f32_e32 v4, v4
	v_exp_f32_e32 v5, v5
	v_add_f32_e32 v3, 1.0, v3
	v_add_f32_e32 v4, 1.0, v4
	v_add_f32_e32 v5, 1.0, v5
	v_rcp_f32_e32 v3, v3
	v_rcp_f32_e32 v4, v4
	v_rcp_f32_e32 v5, v5
	v_fmac_f32_e32 v218, v232, v3
	v_fmac_f32_e32 v219, v232, v4
	v_fmac_f32_e32 v230, v232, v5
	s_andn2_b64 vcc, exec, s[12:13]
	s_cbranch_vccnz .LBB1_6
	v_and_b32_e32 v1, 64, v229
	v_xor_b32_e32 v0, 32, v229
	v_add_u32_e32 v2, 64, v1
	v_cmp_lt_i32_e32 vcc, v0, v2
	s_nop 1
	v_cndmask_b32_e32 v0, v229, v0, vcc
	v_lshlrev_b32_e32 v0, 2, v0
	s_waitcnt lgkmcnt(0)
	ds_bpermute_b32 v1, v0, v230
	v_xor_b32_e32 v3, 16, v229
	v_cmp_lt_i32_e32 vcc, v3, v2
	ds_bpermute_b32 v4, v0, v218
	ds_bpermute_b32 v5, v0, v219
	v_cndmask_b32_e32 v3, v229, v3, vcc
	v_lshlrev_b32_e32 v3, 2, v3
	s_waitcnt lgkmcnt(2)
	v_add_f32_e32 v1, v230, v1
	ds_bpermute_b32 v6, v3, v1
	v_xor_b32_e32 v0, 8, v229
	v_cmp_lt_i32_e32 vcc, v0, v2
	v_xor_b32_e32 v9, 4, v229
	s_waitcnt lgkmcnt(0)
	v_add_f32_e32 v6, v1, v6
	v_cndmask_b32_e32 v0, v229, v0, vcc
	v_lshlrev_b32_e32 v7, 2, v0
	v_pk_add_f32 v[0:1], v[218:219], v[4:5]
	ds_bpermute_b32 v4, v3, v0
	ds_bpermute_b32 v5, v3, v1
	ds_bpermute_b32 v8, v7, v6
	v_cmp_lt_i32_e32 vcc, v9, v2
	s_waitcnt lgkmcnt(1)
	v_pk_add_f32 v[0:1], v[0:1], v[4:5]
	ds_bpermute_b32 v4, v7, v0
	ds_bpermute_b32 v5, v7, v1
	v_cndmask_b32_e32 v3, v229, v9, vcc
	s_waitcnt lgkmcnt(2)
	v_add_f32_e32 v6, v6, v8
	v_lshlrev_b32_e32 v3, 2, v3
	ds_bpermute_b32 v8, v3, v6
	s_waitcnt lgkmcnt(1)
	v_pk_add_f32 v[0:1], v[0:1], v[4:5]
	ds_bpermute_b32 v4, v3, v0
	ds_bpermute_b32 v5, v3, v1
	v_xor_b32_e32 v3, 2, v229
	v_cmp_lt_i32_e32 vcc, v3, v2
	s_waitcnt lgkmcnt(2)
	v_add_f32_e32 v6, v6, v8
	s_waitcnt lgkmcnt(0)
	v_pk_add_f32 v[0:1], v[0:1], v[4:5]
	v_cndmask_b32_e32 v3, v229, v3, vcc
	v_lshlrev_b32_e32 v3, 2, v3
	ds_bpermute_b32 v4, v3, v0
	ds_bpermute_b32 v5, v3, v1
	ds_bpermute_b32 v3, v3, v6
	s_waitcnt lgkmcnt(1)
	v_pk_add_f32 v[0:1], v[0:1], v[4:5]
	s_waitcnt lgkmcnt(0)
	v_add_f32_e32 v4, v6, v3
	v_xor_b32_e32 v3, 1, v229
	v_cmp_lt_i32_e32 vcc, v3, v2
	s_nop 1
	v_cndmask_b32_e32 v2, v229, v3, vcc
	v_lshlrev_b32_e32 v5, 2, v2
	ds_bpermute_b32 v2, v5, v0
	ds_bpermute_b32 v3, v5, v1
	ds_bpermute_b32 v5, v5, v4
	s_and_saveexec_b64 s[12:13], s[2:3]
	s_cbranch_execz .LBB1_5
	v_lshl_add_u32 v6, v231, 1, v231
	v_ashrrev_i32_e32 v7, 31, v6
	s_waitcnt lgkmcnt(0)
	v_add_f32_e32 v4, v4, v5
	v_lshl_add_u64 v[6:7], v[6:7], 2, s[8:9]
	v_pk_add_f32 v[2:3], v[0:1], v[2:3]
	global_store_dwordx3 v[6:7], v[2:4], off
	s_branch .LBB1_5
